# P9 gelu_tanh chain folded to x - x*rcp(exp2(K x (1+c x^2))+1): 5 VALU fewer per element (62 of 64 sites)
# speedup vs baseline: 1.0122x; 1.0056x over previous
.LBB0_1466:
	v_add_u32_e32 v116, v171, v69
	v_add_u32_e32 v119, 0x800, v116
	ds_read2_b64 v[120:123], v119 offset0:224 offset1:240
	s_waitcnt lgkmcnt(0)
	v_pk_fma_f32 v[112:113], v[112:113], 0, v[114:115] op_sel_hi:[1,0,1]
	s_ashr_i32 s43, s42, 31
	v_pk_fma_f32 v[100:101], v[112:113], v[100:101], v[102:103]
	s_andn2_b64 vcc, exec, s[46:47]
	v_lshlrev_b32_e32 v114, 16, v122
	v_lshlrev_b32_e32 v124, 16, v123
	v_and_b32_e32 v115, 0xffff0000, v122
	v_add_f32_e32 v122, 0, v114
	v_exp_f32_e32 v117, v114
	v_exp_f32_e32 v118, v124
	v_and_b32_e32 v114, 0xffff0000, v123
	v_lshlrev_b32_e32 v123, 16, v120
	v_lshlrev_b32_e32 v125, 16, v121
	v_add_f32_e32 v128, v122, v123
	v_add_f32_e32 v124, 0, v124
	v_exp_f32_e32 v130, v123
	v_add_f32_e32 v129, v124, v125
	v_exp_f32_e32 v131, v125
	ds_read2_b64 v[122:125], v119 offset0:192 offset1:208
	v_fma_f32 v126, 0, v117, v115
	v_and_b32_e32 v120, 0xffff0000, v120
	v_fma_f32 v127, 0, v118, v114
	v_fmac_f32_e32 v120, v130, v126
	v_and_b32_e32 v121, 0xffff0000, v121
	s_waitcnt lgkmcnt(0)
	v_lshlrev_b32_e32 v126, 16, v124
	v_fmac_f32_e32 v121, v131, v127
	v_lshlrev_b32_e32 v127, 16, v125
	v_add_f32_e32 v128, v128, v126
	v_add_f32_e32 v129, v129, v127
	v_exp_f32_e32 v126, v126
	v_exp_f32_e32 v127, v127
	v_and_b32_e32 v130, 0xffff0000, v124
	v_fmac_f32_e32 v130, v126, v120
	v_and_b32_e32 v120, 0xffff0000, v125
	v_fmac_f32_e32 v120, v127, v121
	v_lshlrev_b32_e32 v121, 16, v122
	v_lshlrev_b32_e32 v124, 16, v123
	v_add_f32_e32 v128, v128, v121
	v_add_f32_e32 v129, v129, v124
	v_exp_f32_e32 v121, v121
	v_exp_f32_e32 v131, v124
	ds_read2_b64 v[124:127], v119 offset0:160 offset1:176
	v_and_b32_e32 v122, 0xffff0000, v122
	v_fmac_f32_e32 v122, v121, v130
	v_and_b32_e32 v121, 0xffff0000, v123
	v_fmac_f32_e32 v121, v131, v120
	s_waitcnt lgkmcnt(0)
	v_lshlrev_b32_e32 v120, 16, v126
	v_lshlrev_b32_e32 v123, 16, v127
	v_add_f32_e32 v128, v128, v120
	v_add_f32_e32 v129, v129, v123
	v_exp_f32_e32 v120, v120
	v_exp_f32_e32 v123, v123
	v_and_b32_e32 v126, 0xffff0000, v126
	v_fmac_f32_e32 v126, v120, v122
	v_and_b32_e32 v127, 0xffff0000, v127
	v_lshlrev_b32_e32 v120, 16, v124
	v_fmac_f32_e32 v127, v123, v121
	v_lshlrev_b32_e32 v121, 16, v125
	v_add_f32_e32 v128, v128, v120
	v_exp_f32_e32 v130, v120
	v_add_f32_e32 v129, v129, v121
	v_exp_f32_e32 v131, v121
	ds_read2_b64 v[120:123], v119 offset0:128 offset1:144
	v_and_b32_e32 v124, 0xffff0000, v124
	v_fmac_f32_e32 v124, v130, v126
	v_and_b32_e32 v125, 0xffff0000, v125
	v_fmac_f32_e32 v125, v131, v127
	s_waitcnt lgkmcnt(0)
	v_lshlrev_b32_e32 v126, 16, v122
	v_lshlrev_b32_e32 v127, 16, v123
	v_add_f32_e32 v128, v128, v126
	v_add_f32_e32 v129, v129, v127
	v_exp_f32_e32 v126, v126
	v_exp_f32_e32 v127, v127
	v_and_b32_e32 v130, 0xffff0000, v122
	v_fmac_f32_e32 v130, v126, v124
	v_and_b32_e32 v126, 0xffff0000, v123
	v_lshlrev_b32_e32 v122, 16, v120
	v_fmac_f32_e32 v126, v127, v125
	v_lshlrev_b32_e32 v123, 16, v121
	v_add_f32_e32 v127, v128, v122
	v_add_f32_e32 v128, v129, v123
	v_exp_f32_e32 v129, v122
	v_exp_f32_e32 v131, v123
	ds_read2_b64 v[122:125], v119 offset0:96 offset1:112
	v_and_b32_e32 v121, 0xffff0000, v121
	v_and_b32_e32 v120, 0xffff0000, v120
	v_fmac_f32_e32 v121, v131, v126
	v_fmac_f32_e32 v120, v129, v130
	s_waitcnt lgkmcnt(0)
	v_lshlrev_b32_e32 v126, 16, v124
	v_lshlrev_b32_e32 v129, 16, v125
	v_add_f32_e32 v127, v127, v126
	v_add_f32_e32 v128, v128, v129
	v_exp_f32_e32 v126, v126
	v_exp_f32_e32 v129, v129
	v_and_b32_e32 v130, 0xffff0000, v124
	v_fmac_f32_e32 v130, v126, v120
	v_and_b32_e32 v120, 0xffff0000, v125
	v_fmac_f32_e32 v120, v129, v121
	v_lshlrev_b32_e32 v121, 16, v122
	v_lshlrev_b32_e32 v124, 16, v123
	v_add_f32_e32 v129, v127, v121
	v_add_f32_e32 v128, v128, v124
	v_exp_f32_e32 v121, v121
	v_exp_f32_e32 v131, v124
	ds_read2_b64 v[124:127], v119 offset0:64 offset1:80
	v_and_b32_e32 v122, 0xffff0000, v122
	v_fmac_f32_e32 v122, v121, v130
	v_and_b32_e32 v121, 0xffff0000, v123
	v_fmac_f32_e32 v121, v131, v120
	s_waitcnt lgkmcnt(0)
	v_lshlrev_b32_e32 v120, 16, v126
	v_lshlrev_b32_e32 v123, 16, v127
	v_add_f32_e32 v129, v129, v120
	v_add_f32_e32 v128, v128, v123
	v_exp_f32_e32 v120, v120
	v_exp_f32_e32 v123, v123
	v_and_b32_e32 v126, 0xffff0000, v126
	v_fmac_f32_e32 v126, v120, v122
	v_and_b32_e32 v127, 0xffff0000, v127
	v_lshlrev_b32_e32 v120, 16, v124
	v_fmac_f32_e32 v127, v123, v121
	v_lshlrev_b32_e32 v121, 16, v125
	v_add_f32_e32 v129, v129, v120
	v_exp_f32_e32 v130, v120
	v_add_f32_e32 v128, v128, v121
	v_exp_f32_e32 v131, v121
	ds_read2_b64 v[120:123], v119 offset0:32 offset1:48
	v_and_b32_e32 v124, 0xffff0000, v124
	v_fmac_f32_e32 v124, v130, v126
	v_and_b32_e32 v125, 0xffff0000, v125
	v_fmac_f32_e32 v125, v131, v127
	s_waitcnt lgkmcnt(0)
	v_lshlrev_b32_e32 v126, 16, v122
	v_lshlrev_b32_e32 v127, 16, v123
	v_add_f32_e32 v129, v129, v126
	v_add_f32_e32 v128, v128, v127
	v_exp_f32_e32 v126, v126
	v_exp_f32_e32 v127, v127
	v_and_b32_e32 v130, 0xffff0000, v122
	v_fmac_f32_e32 v130, v126, v124
	v_and_b32_e32 v126, 0xffff0000, v123
	v_lshlrev_b32_e32 v122, 16, v120
	v_fmac_f32_e32 v126, v127, v125
	v_lshlrev_b32_e32 v123, 16, v121
	v_add_f32_e32 v127, v129, v122
	v_exp_f32_e32 v129, v122
	v_add_f32_e32 v128, v128, v123
	v_exp_f32_e32 v131, v123
	ds_read2_b64 v[122:125], v119 offset1:16
	v_and_b32_e32 v119, 0xffff0000, v120
	v_and_b32_e32 v120, 0xffff0000, v121
	v_fmac_f32_e32 v120, v131, v126
	v_fmac_f32_e32 v119, v129, v130
	s_waitcnt lgkmcnt(0)
	v_lshlrev_b32_e32 v121, 16, v124
	v_lshlrev_b32_e32 v126, 16, v125
	v_add_f32_e32 v127, v127, v121
	v_add_f32_e32 v128, v128, v126
	v_exp_f32_e32 v121, v121
	v_exp_f32_e32 v126, v126
	v_and_b32_e32 v129, 0xffff0000, v124
	v_fmac_f32_e32 v129, v121, v119
	v_and_b32_e32 v119, 0xffff0000, v125
	v_fmac_f32_e32 v119, v126, v120
	v_lshlrev_b32_e32 v120, 16, v122
	v_lshlrev_b32_e32 v121, 16, v123
	v_add_f32_e32 v130, v127, v120
	v_add_f32_e32 v128, v128, v121
	v_exp_f32_e32 v120, v120
	ds_read2_b64 v[124:127], v116 offset0:224 offset1:240
	v_exp_f32_e32 v121, v121
	v_and_b32_e32 v122, 0xffff0000, v122
	v_fmac_f32_e32 v122, v120, v129
	v_and_b32_e32 v120, 0xffff0000, v123
	v_fmac_f32_e32 v120, v121, v119
	s_waitcnt lgkmcnt(0)
	v_lshlrev_b32_e32 v119, 16, v126
	v_lshlrev_b32_e32 v121, 16, v127
	v_add_f32_e32 v123, v130, v119
	v_add_f32_e32 v128, v128, v121
	v_exp_f32_e32 v119, v119
	v_exp_f32_e32 v121, v121
	v_and_b32_e32 v126, 0xffff0000, v126
	v_fmac_f32_e32 v126, v119, v122
	v_and_b32_e32 v119, 0xffff0000, v127
	v_fmac_f32_e32 v119, v121, v120
	v_lshlrev_b32_e32 v120, 16, v124
	v_lshlrev_b32_e32 v121, 16, v125
	v_add_f32_e32 v127, v123, v120
	v_exp_f32_e32 v129, v120
	v_add_f32_e32 v128, v128, v121
	v_exp_f32_e32 v130, v121
	ds_read2_b64 v[120:123], v116 offset0:192 offset1:208
	v_and_b32_e32 v125, 0xffff0000, v125
	v_and_b32_e32 v124, 0xffff0000, v124
	v_fmac_f32_e32 v125, v130, v119
	v_fmac_f32_e32 v124, v129, v126
	s_waitcnt lgkmcnt(0)
	v_lshlrev_b32_e32 v119, 16, v122
	v_lshlrev_b32_e32 v126, 16, v123
	v_add_f32_e32 v127, v127, v119
	v_add_f32_e32 v128, v128, v126
	v_exp_f32_e32 v119, v119
	v_exp_f32_e32 v126, v126
	v_and_b32_e32 v129, 0xffff0000, v122
	v_fmac_f32_e32 v129, v119, v124
	v_and_b32_e32 v119, 0xffff0000, v123
	v_lshlrev_b32_e32 v122, 16, v120
	v_fmac_f32_e32 v119, v126, v125
	v_lshlrev_b32_e32 v123, 16, v121
	v_add_f32_e32 v126, v127, v122
	v_add_f32_e32 v127, v128, v123
	v_exp_f32_e32 v128, v122
	v_exp_f32_e32 v130, v123
	ds_read2_b64 v[122:125], v116 offset0:160 offset1:176
	v_and_b32_e32 v121, 0xffff0000, v121
	v_and_b32_e32 v120, 0xffff0000, v120
	v_fmac_f32_e32 v121, v130, v119
	v_fmac_f32_e32 v120, v128, v129
	s_waitcnt lgkmcnt(0)
	v_lshlrev_b32_e32 v119, 16, v124
	v_lshlrev_b32_e32 v128, 16, v125
	v_add_f32_e32 v126, v126, v119
	v_add_f32_e32 v127, v127, v128
	v_exp_f32_e32 v119, v119
	v_exp_f32_e32 v128, v128
	v_and_b32_e32 v129, 0xffff0000, v124
	v_fmac_f32_e32 v129, v119, v120
	v_and_b32_e32 v119, 0xffff0000, v125
	v_lshlrev_b32_e32 v120, 16, v122
	v_fmac_f32_e32 v119, v128, v121
	v_lshlrev_b32_e32 v121, 16, v123
	v_add_f32_e32 v128, v126, v120
	v_add_f32_e32 v130, v127, v121
	v_exp_f32_e32 v120, v120
	ds_read2_b64 v[124:127], v116 offset0:128 offset1:144
	v_exp_f32_e32 v121, v121
	v_and_b32_e32 v122, 0xffff0000, v122
	v_fmac_f32_e32 v122, v120, v129
	v_and_b32_e32 v120, 0xffff0000, v123
	v_fmac_f32_e32 v120, v121, v119
	s_waitcnt lgkmcnt(0)
	v_lshlrev_b32_e32 v119, 16, v126
	v_lshlrev_b32_e32 v121, 16, v127
	v_add_f32_e32 v123, v128, v119
	v_add_f32_e32 v128, v130, v121
	v_exp_f32_e32 v119, v119
	v_exp_f32_e32 v121, v121
	v_and_b32_e32 v126, 0xffff0000, v126
	v_fmac_f32_e32 v126, v119, v122
	v_and_b32_e32 v119, 0xffff0000, v127
	v_fmac_f32_e32 v119, v121, v120
	v_lshlrev_b32_e32 v120, 16, v124
	v_lshlrev_b32_e32 v121, 16, v125
	v_add_f32_e32 v127, v123, v120
	v_exp_f32_e32 v129, v120
	v_add_f32_e32 v128, v128, v121
	v_exp_f32_e32 v130, v121
	ds_read2_b64 v[120:123], v116 offset0:96 offset1:112
	v_and_b32_e32 v125, 0xffff0000, v125
	v_and_b32_e32 v124, 0xffff0000, v124
	v_fmac_f32_e32 v125, v130, v119
	v_fmac_f32_e32 v124, v129, v126
	s_waitcnt lgkmcnt(0)
	v_lshlrev_b32_e32 v119, 16, v122
	v_lshlrev_b32_e32 v126, 16, v123
	v_add_f32_e32 v127, v127, v119
	v_add_f32_e32 v128, v128, v126
	v_exp_f32_e32 v119, v119
	v_exp_f32_e32 v126, v126
	v_and_b32_e32 v129, 0xffff0000, v122
	v_fmac_f32_e32 v129, v119, v124
	v_and_b32_e32 v119, 0xffff0000, v123
	v_lshlrev_b32_e32 v122, 16, v120
	v_fmac_f32_e32 v119, v126, v125
	v_lshlrev_b32_e32 v123, 16, v121
	v_add_f32_e32 v126, v127, v122
	v_add_f32_e32 v127, v128, v123
	v_exp_f32_e32 v128, v122
	v_exp_f32_e32 v130, v123
	ds_read2_b64 v[122:125], v116 offset0:64 offset1:80
	v_and_b32_e32 v121, 0xffff0000, v121
	v_and_b32_e32 v120, 0xffff0000, v120
	v_fmac_f32_e32 v121, v130, v119
	v_fmac_f32_e32 v120, v128, v129
	s_waitcnt lgkmcnt(0)
	v_lshlrev_b32_e32 v119, 16, v124
	v_lshlrev_b32_e32 v128, 16, v125
	v_add_f32_e32 v126, v126, v119
	v_add_f32_e32 v127, v127, v128
	v_exp_f32_e32 v119, v119
	v_exp_f32_e32 v128, v128
	v_and_b32_e32 v129, 0xffff0000, v124
	v_fmac_f32_e32 v129, v119, v120
	v_and_b32_e32 v119, 0xffff0000, v125
	v_lshlrev_b32_e32 v120, 16, v122
	v_fmac_f32_e32 v119, v128, v121
	v_lshlrev_b32_e32 v121, 16, v123
	v_add_f32_e32 v128, v126, v120
	v_add_f32_e32 v130, v127, v121
	v_exp_f32_e32 v120, v120
	ds_read2_b64 v[124:127], v116 offset0:32 offset1:48
	v_exp_f32_e32 v121, v121
	v_and_b32_e32 v122, 0xffff0000, v122
	v_fmac_f32_e32 v122, v120, v129
	v_and_b32_e32 v120, 0xffff0000, v123
	v_fmac_f32_e32 v120, v121, v119
	s_waitcnt lgkmcnt(0)
	v_lshlrev_b32_e32 v119, 16, v126
	v_lshlrev_b32_e32 v121, 16, v127
	v_add_f32_e32 v123, v128, v119
	v_add_f32_e32 v128, v130, v121
	v_exp_f32_e32 v119, v119
	v_exp_f32_e32 v121, v121
	v_and_b32_e32 v126, 0xffff0000, v126
	v_fmac_f32_e32 v126, v119, v122
	v_and_b32_e32 v119, 0xffff0000, v127
	v_fmac_f32_e32 v119, v121, v120
	v_lshlrev_b32_e32 v120, 16, v124
	v_lshlrev_b32_e32 v121, 16, v125
	v_add_f32_e32 v127, v123, v120
	v_exp_f32_e32 v129, v120
	v_add_f32_e32 v128, v128, v121
	v_exp_f32_e32 v130, v121
	ds_read2_b64 v[120:123], v116 offset1:16
	v_and_b32_e32 v125, 0xffff0000, v125
	v_and_b32_e32 v124, 0xffff0000, v124
	v_fmac_f32_e32 v125, v130, v119
	v_fmac_f32_e32 v124, v129, v126
	s_waitcnt lgkmcnt(0)
	v_lshlrev_b32_e32 v119, 16, v122
	v_lshlrev_b32_e32 v126, 16, v123
	v_add_f32_e32 v127, v127, v119
	v_add_f32_e32 v128, v128, v126
	v_exp_f32_e32 v119, v119
	v_exp_f32_e32 v126, v126
	v_and_b32_e32 v122, 0xffff0000, v122
	v_fmac_f32_e32 v122, v119, v124
	v_and_b32_e32 v119, 0xffff0000, v123
	v_lshlrev_b32_e32 v123, 16, v120
	v_fmac_f32_e32 v119, v126, v125
	v_exp_f32_e32 v125, v123
	v_lshlrev_b32_e32 v124, 16, v121
	v_add_f32_e32 v123, v127, v123
	v_and_b32_e32 v120, 0xffff0000, v120
	v_fmac_f32_e32 v120, v125, v122
	v_exp_f32_e32 v122, v124
	v_exp_f32_e32 v123, v123
	v_and_b32_e32 v121, 0xffff0000, v121
	ds_bpermute_b32 v125, v168, v120
	v_fmac_f32_e32 v121, v122, v119
	ds_bpermute_b32 v119, v168, v123
	ds_bpermute_b32 v102, v167, v123
	ds_bpermute_b32 v103, v167, v120
	v_pk_fma_f32 v[100:101], v[100:101], v[104:105], v[106:107]
	ds_bpermute_b32 v107, v166, v120
	v_pk_fma_f32 v[100:101], v[100:101], v[108:109], v[110:111]
	v_add_f32_e32 v126, v128, v124
	s_waitcnt lgkmcnt(3)
	v_fmac_f32_e32 v125, v100, v119
	v_cndmask_b32_e64 v100, v125, v100, s[6:7]
	s_waitcnt lgkmcnt(1)
	v_fmac_f32_e32 v103, v100, v102
	ds_bpermute_b32 v102, v166, v123
	v_cndmask_b32_e64 v100, v100, v103, s[8:9]
	v_exp_f32_e32 v124, v126
	ds_bpermute_b32 v126, v168, v121
	s_waitcnt lgkmcnt(1)
	v_fmac_f32_e32 v107, v100, v102
	s_waitcnt vmcnt(16)
	v_lshlrev_b32_e32 v102, 16, v236
	v_mul_f32_e32 v103, 0x3d372713, v102
	v_mul_f32_e32 v103, v103, v102
	v_fma_f32 v103, v103, v102, v102
	v_mul_f32_e32 v103, 0x40135761, v103
	ds_bpermute_b32 v122, v168, v124
	ds_bpermute_b32 v104, v167, v124
	ds_bpermute_b32 v105, v167, v121
	v_exp_f32_e32 v103, v103
	s_waitcnt lgkmcnt(2)
	v_fmac_f32_e32 v126, v101, v122
	v_cndmask_b32_e64 v100, v100, v107, s[0:1]
	v_cndmask_b32_e64 v101, v126, v101, s[6:7]
	v_fmac_f32_e32 v115, v117, v100
	v_add_f32_e32 v100, 1.0, v103
	v_and_b32_e32 v103, 0xffff0000, v236
	s_waitcnt lgkmcnt(0)
	v_fmac_f32_e32 v105, v101, v104
	v_mul_f32_e32 v104, 0x3d372713, v103
	v_mul_f32_e32 v104, v104, v103
	v_fma_f32 v104, v104, v103, v103
	v_mul_f32_e32 v104, 0x40135761, v104
	v_rcp_f32_e32 v100, v100
	v_exp_f32_e32 v104, v104
	ds_bpermute_b32 v106, v166, v124
	ds_bpermute_b32 v108, v166, v121
	v_fma_f32 v100, -v102, v100, v102
	v_add_f32_e32 v102, 1.0, v104
	v_cndmask_b32_e64 v101, v101, v105, s[8:9]
	v_rcp_f32_e32 v102, v102
	s_waitcnt lgkmcnt(0)
	v_fmac_f32_e32 v108, v101, v106
	v_cndmask_b32_e64 v101, v101, v108, s[0:1]
	v_fmac_f32_e32 v114, v118, v101
	v_lshlrev_b32_e32 v101, 16, v233
	v_add_f32_e32 v101, v115, v101
	v_mul_f32_e32 v100, v100, v101
	v_and_b32_e32 v101, 0xffff0000, v233
	v_add_f32_e32 v101, v114, v101
	v_fma_f32 v102, -v103, v102, v103
	v_mul_f32_e32 v101, v102, v101
	v_cvt_pk_bf16_f32 v102, v100, v101
	ds_read_b64 v[100:101], v116 offset:3840
	ds_write_b32 v190, v102 offset:3968
	s_add_i32 s34, s34, s35
	s_waitcnt lgkmcnt(1)
	v_lshlrev_b32_e32 v103, 16, v100
	v_exp_f32_e32 v103, v103
	v_and_b32_e32 v102, 0xffff0000, v100
	v_lshlrev_b32_e32 v100, 16, v101
	v_and_b32_e32 v105, 0xffff0000, v101
	v_fmac_f32_e32 v102, v115, v103
	v_lshlrev_b32_e32 v103, 16, v235
	v_mul_f32_e32 v104, 0x3d372713, v103
	v_mul_f32_e32 v104, v104, v103
	v_fma_f32 v104, v104, v103, v103
	v_mul_f32_e32 v104, 0x40135761, v104
	v_exp_f32_e32 v104, v104
	v_exp_f32_e32 v100, v100
	v_add_f32_e32 v101, 1.0, v104
	v_and_b32_e32 v104, 0xffff0000, v235
	v_mul_f32_e32 v106, 0x3d372713, v104
	v_mul_f32_e32 v106, v106, v104
	v_fma_f32 v106, v106, v104, v104
	v_mul_f32_e32 v106, 0x40135761, v106
	v_rcp_f32_e32 v101, v101
	v_exp_f32_e32 v106, v106
	v_fma_f32 v101, -v103, v101, v103
	v_add_f32_e32 v103, 1.0, v106
	v_rcp_f32_e32 v103, v103
	v_fmac_f32_e32 v105, v114, v100
	v_lshlrev_b32_e32 v100, 16, v231
	v_add_f32_e32 v100, v102, v100
	v_mul_f32_e32 v100, v101, v100
	v_and_b32_e32 v101, 0xffff0000, v231
	v_add_f32_e32 v101, v105, v101
	v_fma_f32 v103, -v104, v103, v104
	v_mul_f32_e32 v101, v103, v101
	v_cvt_pk_bf16_f32 v103, v100, v101
	ds_read_b64 v[100:101], v116 offset:3712
	ds_write_b32 v190, v103 offset:3840
	s_waitcnt lgkmcnt(1)
	v_lshlrev_b32_e32 v104, 16, v100
	v_exp_f32_e32 v104, v104
	v_and_b32_e32 v103, 0xffff0000, v100
	v_lshlrev_b32_e32 v100, 16, v101
	v_fmac_f32_e32 v103, v102, v104
	v_lshlrev_b32_e32 v102, 16, v234
	v_mul_f32_e32 v104, 0x3d372713, v102
	v_mul_f32_e32 v104, v104, v102
	v_fma_f32 v104, v104, v102, v102
	v_mul_f32_e32 v104, 0x40135761, v104
	v_exp_f32_e32 v104, v104
	v_exp_f32_e32 v100, v100
	v_and_b32_e32 v106, 0xffff0000, v101
	v_add_f32_e32 v101, 1.0, v104
	v_and_b32_e32 v104, 0xffff0000, v234
	v_fmac_f32_e32 v106, v105, v100
	v_mul_f32_e32 v105, 0x3d372713, v104
	v_mul_f32_e32 v105, v105, v104
	v_fma_f32 v105, v105, v104, v104
	v_mul_f32_e32 v105, 0x40135761, v105
	v_rcp_f32_e32 v101, v101
	v_exp_f32_e32 v105, v105
	v_fma_f32 v101, -v102, v101, v102
	v_add_f32_e32 v102, 1.0, v105
	v_rcp_f32_e32 v102, v102
	v_lshlrev_b32_e32 v100, 16, v229
	v_add_f32_e32 v100, v103, v100
	v_mul_f32_e32 v100, v101, v100
	v_and_b32_e32 v101, 0xffff0000, v229
	v_add_f32_e32 v101, v106, v101
	v_fma_f32 v102, -v104, v102, v104
	v_mul_f32_e32 v101, v102, v101
	v_cvt_pk_bf16_f32 v102, v100, v101
	ds_read_b64 v[100:101], v116 offset:3584
	ds_write_b32 v190, v102 offset:3712
	s_waitcnt lgkmcnt(1)
	v_lshlrev_b32_e32 v104, 16, v100
	v_exp_f32_e32 v104, v104
	v_and_b32_e32 v102, 0xffff0000, v100
	v_lshlrev_b32_e32 v100, 16, v101
	v_fmac_f32_e32 v102, v103, v104
	v_lshlrev_b32_e32 v103, 16, v232
	v_mul_f32_e32 v104, 0x3d372713, v103
	v_mul_f32_e32 v104, v104, v103
	v_fma_f32 v104, v104, v103, v103
	v_mul_f32_e32 v104, 0x40135761, v104
	v_exp_f32_e32 v104, v104
	v_exp_f32_e32 v100, v100
	v_and_b32_e32 v105, 0xffff0000, v101
	v_add_f32_e32 v101, 1.0, v104
	v_and_b32_e32 v104, 0xffff0000, v232
	v_fmac_f32_e32 v105, v106, v100
	v_mul_f32_e32 v106, 0x3d372713, v104
	v_mul_f32_e32 v106, v106, v104
	v_fma_f32 v106, v106, v104, v104
	v_mul_f32_e32 v106, 0x40135761, v106
	v_rcp_f32_e32 v101, v101
	v_exp_f32_e32 v106, v106
	v_fma_f32 v101, -v103, v101, v103
	v_add_f32_e32 v103, 1.0, v106
	v_rcp_f32_e32 v103, v103
	v_lshlrev_b32_e32 v100, 16, v227
	v_add_f32_e32 v100, v102, v100
	v_mul_f32_e32 v100, v101, v100
	v_and_b32_e32 v101, 0xffff0000, v227
	v_add_f32_e32 v101, v105, v101
	v_fma_f32 v103, -v104, v103, v104
	v_mul_f32_e32 v101, v103, v101
	v_cvt_pk_bf16_f32 v103, v100, v101
	ds_read_b64 v[100:101], v116 offset:3456
	ds_write_b32 v190, v103 offset:3584
	s_waitcnt lgkmcnt(1)
	v_lshlrev_b32_e32 v104, 16, v100
	v_exp_f32_e32 v104, v104
	v_and_b32_e32 v103, 0xffff0000, v100
	v_lshlrev_b32_e32 v100, 16, v101
	v_fmac_f32_e32 v103, v102, v104
	v_lshlrev_b32_e32 v102, 16, v230
	v_mul_f32_e32 v104, 0x3d372713, v102
	v_mul_f32_e32 v104, v104, v102
	v_fma_f32 v104, v104, v102, v102
	v_mul_f32_e32 v104, 0x40135761, v104
	v_exp_f32_e32 v104, v104
	v_exp_f32_e32 v100, v100
	v_and_b32_e32 v106, 0xffff0000, v101
	v_add_f32_e32 v101, 1.0, v104
	v_and_b32_e32 v104, 0xffff0000, v230
	v_fmac_f32_e32 v106, v105, v100
	v_mul_f32_e32 v105, 0x3d372713, v104
	v_mul_f32_e32 v105, v105, v104
	v_fma_f32 v105, v105, v104, v104
	v_mul_f32_e32 v105, 0x40135761, v105
	v_rcp_f32_e32 v101, v101
	v_exp_f32_e32 v105, v105
	v_fma_f32 v101, -v102, v101, v102
	v_add_f32_e32 v102, 1.0, v105
	v_rcp_f32_e32 v102, v102
	v_lshlrev_b32_e32 v100, 16, v225
	v_add_f32_e32 v100, v103, v100
	v_mul_f32_e32 v100, v101, v100
	v_and_b32_e32 v101, 0xffff0000, v225
	v_add_f32_e32 v101, v106, v101
	v_fma_f32 v102, -v104, v102, v104
	v_mul_f32_e32 v101, v102, v101
	v_cvt_pk_bf16_f32 v102, v100, v101
	ds_read_b64 v[100:101], v116 offset:3328
	ds_write_b32 v190, v102 offset:3456
	s_waitcnt lgkmcnt(1)
	v_lshlrev_b32_e32 v104, 16, v100
	v_exp_f32_e32 v104, v104
	v_and_b32_e32 v102, 0xffff0000, v100
	v_lshlrev_b32_e32 v100, 16, v101
	v_fmac_f32_e32 v102, v103, v104
	v_lshlrev_b32_e32 v103, 16, v228
	v_mul_f32_e32 v104, 0x3d372713, v103
	v_mul_f32_e32 v104, v104, v103
	v_fma_f32 v104, v104, v103, v103
	v_mul_f32_e32 v104, 0x40135761, v104
	v_exp_f32_e32 v104, v104
	v_exp_f32_e32 v100, v100
	v_and_b32_e32 v105, 0xffff0000, v101
	v_add_f32_e32 v101, 1.0, v104
	v_and_b32_e32 v104, 0xffff0000, v228
	v_fmac_f32_e32 v105, v106, v100
	v_mul_f32_e32 v106, 0x3d372713, v104
	v_mul_f32_e32 v106, v106, v104
	v_fma_f32 v106, v106, v104, v104
	v_mul_f32_e32 v106, 0x40135761, v106
	v_rcp_f32_e32 v101, v101
	v_exp_f32_e32 v106, v106
	v_fma_f32 v101, -v103, v101, v103
	v_add_f32_e32 v103, 1.0, v106
	v_rcp_f32_e32 v103, v103
	v_lshlrev_b32_e32 v100, 16, v222
	v_add_f32_e32 v100, v102, v100
	v_mul_f32_e32 v100, v101, v100
	v_and_b32_e32 v101, 0xffff0000, v222
	v_add_f32_e32 v101, v105, v101
	v_fma_f32 v103, -v104, v103, v104
	v_mul_f32_e32 v101, v103, v101
	v_cvt_pk_bf16_f32 v103, v100, v101
	ds_read_b64 v[100:101], v116 offset:3200
	ds_write_b32 v190, v103 offset:3328
	s_waitcnt lgkmcnt(1)
	v_lshlrev_b32_e32 v104, 16, v100
	v_exp_f32_e32 v104, v104
	v_and_b32_e32 v103, 0xffff0000, v100
	v_lshlrev_b32_e32 v100, 16, v101
	v_fmac_f32_e32 v103, v102, v104
	v_lshlrev_b32_e32 v102, 16, v226
	v_mul_f32_e32 v104, 0x3d372713, v102
	v_mul_f32_e32 v104, v104, v102
	v_fma_f32 v104, v104, v102, v102
	v_mul_f32_e32 v104, 0x40135761, v104
	v_exp_f32_e32 v104, v104
	v_exp_f32_e32 v100, v100
	v_and_b32_e32 v106, 0xffff0000, v101
	v_add_f32_e32 v101, 1.0, v104
	v_and_b32_e32 v104, 0xffff0000, v226
	v_fmac_f32_e32 v106, v105, v100
	v_mul_f32_e32 v105, 0x3d372713, v104
	v_mul_f32_e32 v105, v105, v104
	v_fma_f32 v105, v105, v104, v104
	v_mul_f32_e32 v105, 0x40135761, v105
	v_rcp_f32_e32 v101, v101
	v_exp_f32_e32 v105, v105
	v_fma_f32 v101, -v102, v101, v102
	v_add_f32_e32 v102, 1.0, v105
	v_rcp_f32_e32 v102, v102
	v_lshlrev_b32_e32 v100, 16, v220
	v_add_f32_e32 v100, v103, v100
	v_mul_f32_e32 v100, v101, v100
	v_and_b32_e32 v101, 0xffff0000, v220
	v_add_f32_e32 v101, v106, v101
	v_fma_f32 v102, -v104, v102, v104
	v_mul_f32_e32 v101, v102, v101
	v_cvt_pk_bf16_f32 v102, v100, v101
	ds_read_b64 v[100:101], v116 offset:3072
	ds_write_b32 v190, v102 offset:3200
	s_waitcnt lgkmcnt(1)
	v_lshlrev_b32_e32 v104, 16, v100
	v_exp_f32_e32 v104, v104
	v_and_b32_e32 v102, 0xffff0000, v100
	v_lshlrev_b32_e32 v100, 16, v101
	v_fmac_f32_e32 v102, v103, v104
	v_lshlrev_b32_e32 v103, 16, v224
	v_mul_f32_e32 v104, 0x3d372713, v103
	v_mul_f32_e32 v104, v104, v103
	v_fma_f32 v104, v104, v103, v103
	v_mul_f32_e32 v104, 0x40135761, v104
	v_exp_f32_e32 v104, v104
	v_exp_f32_e32 v100, v100
	v_and_b32_e32 v105, 0xffff0000, v101
	v_add_f32_e32 v101, 1.0, v104
	v_and_b32_e32 v104, 0xffff0000, v224
	v_fmac_f32_e32 v105, v106, v100
	v_mul_f32_e32 v106, 0x3d372713, v104
	v_mul_f32_e32 v106, v106, v104
	v_fma_f32 v106, v106, v104, v104
	v_mul_f32_e32 v106, 0x40135761, v106
	v_rcp_f32_e32 v101, v101
	v_exp_f32_e32 v106, v106
	v_fma_f32 v101, -v103, v101, v103
	v_add_f32_e32 v103, 1.0, v106
	v_rcp_f32_e32 v103, v103
	v_lshlrev_b32_e32 v100, 16, v218
	v_add_f32_e32 v100, v102, v100
	v_mul_f32_e32 v100, v101, v100
	v_and_b32_e32 v101, 0xffff0000, v218
	v_add_f32_e32 v101, v105, v101
	v_fma_f32 v103, -v104, v103, v104
	v_mul_f32_e32 v101, v103, v101
	v_cvt_pk_bf16_f32 v103, v100, v101
	ds_read_b64 v[100:101], v116 offset:2944
	ds_write_b32 v190, v103 offset:3072
	s_waitcnt lgkmcnt(1)
	v_lshlrev_b32_e32 v104, 16, v100
	v_exp_f32_e32 v104, v104
	v_and_b32_e32 v103, 0xffff0000, v100
	v_lshlrev_b32_e32 v100, 16, v101
	v_fmac_f32_e32 v103, v102, v104
	v_lshlrev_b32_e32 v102, 16, v223
	v_mul_f32_e32 v104, 0x3d372713, v102
	v_mul_f32_e32 v104, v104, v102
	v_fma_f32 v104, v104, v102, v102
	v_mul_f32_e32 v104, 0x40135761, v104
	v_exp_f32_e32 v104, v104
	v_exp_f32_e32 v100, v100
	v_and_b32_e32 v106, 0xffff0000, v101
	v_add_f32_e32 v101, 1.0, v104
	v_and_b32_e32 v104, 0xffff0000, v223
	v_fmac_f32_e32 v106, v105, v100
	v_mul_f32_e32 v105, 0x3d372713, v104
	v_mul_f32_e32 v105, v105, v104
	v_fma_f32 v105, v105, v104, v104
	v_mul_f32_e32 v105, 0x40135761, v105
	v_rcp_f32_e32 v101, v101
	v_exp_f32_e32 v105, v105
	v_fma_f32 v101, -v102, v101, v102
	v_add_f32_e32 v102, 1.0, v105
	v_rcp_f32_e32 v102, v102
	v_lshlrev_b32_e32 v100, 16, v216
	v_add_f32_e32 v100, v103, v100
	v_mul_f32_e32 v100, v101, v100
	v_and_b32_e32 v101, 0xffff0000, v216
	v_add_f32_e32 v101, v106, v101
	v_fma_f32 v102, -v104, v102, v104
	v_mul_f32_e32 v101, v102, v101
	v_cvt_pk_bf16_f32 v102, v100, v101
	ds_read_b64 v[100:101], v116 offset:2816
	ds_write_b32 v190, v102 offset:2944
	s_waitcnt lgkmcnt(1)
	v_lshlrev_b32_e32 v104, 16, v100
	v_exp_f32_e32 v104, v104
	v_and_b32_e32 v102, 0xffff0000, v100
	v_lshlrev_b32_e32 v100, 16, v101
	v_fmac_f32_e32 v102, v103, v104
	v_lshlrev_b32_e32 v103, 16, v221
	v_mul_f32_e32 v104, 0x3d372713, v103
	v_mul_f32_e32 v104, v104, v103
	v_fma_f32 v104, v104, v103, v103
	v_mul_f32_e32 v104, 0x40135761, v104
	v_exp_f32_e32 v104, v104
	v_exp_f32_e32 v100, v100
	v_and_b32_e32 v105, 0xffff0000, v101
	v_add_f32_e32 v101, 1.0, v104
	v_and_b32_e32 v104, 0xffff0000, v221
	v_fmac_f32_e32 v105, v106, v100
	v_mul_f32_e32 v106, 0x3d372713, v104
	v_mul_f32_e32 v106, v106, v104
	v_fma_f32 v106, v106, v104, v104
	v_mul_f32_e32 v106, 0x40135761, v106
	v_rcp_f32_e32 v101, v101
	v_exp_f32_e32 v106, v106
	v_fma_f32 v101, -v103, v101, v103
	v_add_f32_e32 v103, 1.0, v106
	v_rcp_f32_e32 v103, v103
	v_lshlrev_b32_e32 v100, 16, v214
	v_add_f32_e32 v100, v102, v100
	v_mul_f32_e32 v100, v101, v100
	v_and_b32_e32 v101, 0xffff0000, v214
	v_add_f32_e32 v101, v105, v101
	v_fma_f32 v103, -v104, v103, v104
	v_mul_f32_e32 v101, v103, v101
	v_cvt_pk_bf16_f32 v103, v100, v101
	ds_read_b64 v[100:101], v116 offset:2688
	ds_write_b32 v190, v103 offset:2816
	s_waitcnt lgkmcnt(1)
	v_lshlrev_b32_e32 v104, 16, v100
	v_exp_f32_e32 v104, v104
	v_and_b32_e32 v103, 0xffff0000, v100
	v_lshlrev_b32_e32 v100, 16, v101
	v_fmac_f32_e32 v103, v102, v104
	v_lshlrev_b32_e32 v102, 16, v219
	v_mul_f32_e32 v104, 0x3d372713, v102
	v_mul_f32_e32 v104, v104, v102
	v_fma_f32 v104, v104, v102, v102
	v_mul_f32_e32 v104, 0x40135761, v104
	v_exp_f32_e32 v104, v104
	v_exp_f32_e32 v100, v100
	v_and_b32_e32 v106, 0xffff0000, v101
	v_add_f32_e32 v101, 1.0, v104
	v_and_b32_e32 v104, 0xffff0000, v219
	v_fmac_f32_e32 v106, v105, v100
	v_mul_f32_e32 v105, 0x3d372713, v104
	v_mul_f32_e32 v105, v105, v104
	v_fma_f32 v105, v105, v104, v104
	v_mul_f32_e32 v105, 0x40135761, v105
	v_rcp_f32_e32 v101, v101
	v_exp_f32_e32 v105, v105
	v_fma_f32 v101, -v102, v101, v102
	v_add_f32_e32 v102, 1.0, v105
	v_rcp_f32_e32 v102, v102
	v_lshlrev_b32_e32 v100, 16, v211
	v_add_f32_e32 v100, v103, v100
	v_mul_f32_e32 v100, v101, v100
	v_and_b32_e32 v101, 0xffff0000, v211
	v_add_f32_e32 v101, v106, v101
	v_fma_f32 v102, -v104, v102, v104
	v_mul_f32_e32 v101, v102, v101
	v_cvt_pk_bf16_f32 v102, v100, v101
	ds_read_b64 v[100:101], v116 offset:2560
	ds_write_b32 v190, v102 offset:2688
	s_waitcnt lgkmcnt(1)
	v_lshlrev_b32_e32 v104, 16, v100
	v_exp_f32_e32 v104, v104
	v_and_b32_e32 v102, 0xffff0000, v100
	v_lshlrev_b32_e32 v100, 16, v101
	v_fmac_f32_e32 v102, v103, v104
	v_lshlrev_b32_e32 v103, 16, v217
	v_mul_f32_e32 v104, 0x3d372713, v103
	v_mul_f32_e32 v104, v104, v103
	v_fma_f32 v104, v104, v103, v103
	v_mul_f32_e32 v104, 0x40135761, v104
	v_exp_f32_e32 v104, v104
	v_exp_f32_e32 v100, v100
	v_and_b32_e32 v105, 0xffff0000, v101
	v_add_f32_e32 v101, 1.0, v104
	v_and_b32_e32 v104, 0xffff0000, v217
	v_fmac_f32_e32 v105, v106, v100
	v_mul_f32_e32 v106, 0x3d372713, v104
	v_mul_f32_e32 v106, v106, v104
	v_fma_f32 v106, v106, v104, v104
	v_mul_f32_e32 v106, 0x40135761, v106
	v_rcp_f32_e32 v101, v101
	v_exp_f32_e32 v106, v106
	v_fma_f32 v101, -v103, v101, v103
	v_add_f32_e32 v103, 1.0, v106
	v_rcp_f32_e32 v103, v103
	v_lshlrev_b32_e32 v100, 16, v209
	v_add_f32_e32 v100, v102, v100
	v_mul_f32_e32 v100, v101, v100
	v_and_b32_e32 v101, 0xffff0000, v209
	v_add_f32_e32 v101, v105, v101
	v_fma_f32 v103, -v104, v103, v104
	v_mul_f32_e32 v101, v103, v101
	v_cvt_pk_bf16_f32 v103, v100, v101
	ds_read_b64 v[100:101], v116 offset:2432
	ds_write_b32 v190, v103 offset:2560
	s_waitcnt lgkmcnt(1)
	v_lshlrev_b32_e32 v104, 16, v100
	v_exp_f32_e32 v104, v104
	v_and_b32_e32 v103, 0xffff0000, v100
	v_lshlrev_b32_e32 v100, 16, v101
	v_fmac_f32_e32 v103, v102, v104
	v_lshlrev_b32_e32 v102, 16, v215
	v_mul_f32_e32 v104, 0x3d372713, v102
	v_mul_f32_e32 v104, v104, v102
	v_fma_f32 v104, v104, v102, v102
	v_mul_f32_e32 v104, 0x40135761, v104
	v_exp_f32_e32 v104, v104
	v_exp_f32_e32 v100, v100
	v_and_b32_e32 v106, 0xffff0000, v101
	v_add_f32_e32 v101, 1.0, v104
	v_and_b32_e32 v104, 0xffff0000, v215
	v_fmac_f32_e32 v106, v105, v100
	v_mul_f32_e32 v105, 0x3d372713, v104
	v_mul_f32_e32 v105, v105, v104
	v_fma_f32 v105, v105, v104, v104
	v_mul_f32_e32 v105, 0x40135761, v105
	v_rcp_f32_e32 v101, v101
	v_exp_f32_e32 v105, v105
	v_fma_f32 v101, -v102, v101, v102
	v_add_f32_e32 v102, 1.0, v105
	v_rcp_f32_e32 v102, v102
	v_lshlrev_b32_e32 v100, 16, v207
	v_add_f32_e32 v100, v103, v100
	v_mul_f32_e32 v100, v101, v100
	v_and_b32_e32 v101, 0xffff0000, v207
	v_add_f32_e32 v101, v106, v101
	v_fma_f32 v102, -v104, v102, v104
	v_mul_f32_e32 v101, v102, v101
	v_cvt_pk_bf16_f32 v102, v100, v101
	ds_read_b64 v[100:101], v116 offset:2304
	ds_write_b32 v190, v102 offset:2432
	s_waitcnt lgkmcnt(1)
	v_lshlrev_b32_e32 v104, 16, v100
	v_exp_f32_e32 v104, v104
	v_and_b32_e32 v102, 0xffff0000, v100
	v_lshlrev_b32_e32 v100, 16, v101
	v_fmac_f32_e32 v102, v103, v104
	v_lshlrev_b32_e32 v103, 16, v213
	v_mul_f32_e32 v104, 0x3d372713, v103
	v_mul_f32_e32 v104, v104, v103
	v_fma_f32 v104, v104, v103, v103
	v_mul_f32_e32 v104, 0x40135761, v104
	v_exp_f32_e32 v104, v104
	v_exp_f32_e32 v100, v100
	v_and_b32_e32 v105, 0xffff0000, v101
	v_add_f32_e32 v101, 1.0, v104
	v_and_b32_e32 v104, 0xffff0000, v213
	v_fmac_f32_e32 v105, v106, v100
	v_mul_f32_e32 v106, 0x3d372713, v104
	v_mul_f32_e32 v106, v106, v104
	v_fma_f32 v106, v106, v104, v104
	v_mul_f32_e32 v106, 0x40135761, v106
	v_rcp_f32_e32 v101, v101
	v_exp_f32_e32 v106, v106
	v_fma_f32 v101, -v103, v101, v103
	v_add_f32_e32 v103, 1.0, v106
	v_rcp_f32_e32 v103, v103
	v_lshlrev_b32_e32 v100, 16, v205
	v_add_f32_e32 v100, v102, v100
	v_mul_f32_e32 v100, v101, v100
	v_and_b32_e32 v101, 0xffff0000, v205
	v_add_f32_e32 v101, v105, v101
	v_fma_f32 v103, -v104, v103, v104
	v_mul_f32_e32 v101, v103, v101
	v_cvt_pk_bf16_f32 v103, v100, v101
	ds_read_b64 v[100:101], v116 offset:2176
	ds_write_b32 v190, v103 offset:2304
	s_waitcnt lgkmcnt(1)
	v_lshlrev_b32_e32 v104, 16, v100
	v_exp_f32_e32 v104, v104
	v_and_b32_e32 v103, 0xffff0000, v100
	v_lshlrev_b32_e32 v100, 16, v101
	v_fmac_f32_e32 v103, v102, v104
	v_lshlrev_b32_e32 v102, 16, v212
	v_mul_f32_e32 v104, 0x3d372713, v102
	v_mul_f32_e32 v104, v104, v102
	v_fma_f32 v104, v104, v102, v102
	v_mul_f32_e32 v104, 0x40135761, v104
	v_exp_f32_e32 v104, v104
	v_exp_f32_e32 v100, v100
	v_and_b32_e32 v106, 0xffff0000, v101
	v_add_f32_e32 v101, 1.0, v104
	v_and_b32_e32 v104, 0xffff0000, v212
	v_fmac_f32_e32 v106, v105, v100
	v_mul_f32_e32 v105, 0x3d372713, v104
	v_mul_f32_e32 v105, v105, v104
	v_fma_f32 v105, v105, v104, v104
	v_mul_f32_e32 v105, 0x40135761, v105
	v_rcp_f32_e32 v101, v101
	v_exp_f32_e32 v105, v105
	v_fma_f32 v101, -v102, v101, v102
	v_add_f32_e32 v102, 1.0, v105
	v_rcp_f32_e32 v102, v102
	v_lshlrev_b32_e32 v100, 16, v203
	v_add_f32_e32 v100, v103, v100
	v_mul_f32_e32 v100, v101, v100
	v_and_b32_e32 v101, 0xffff0000, v203
	v_add_f32_e32 v101, v106, v101
	v_fma_f32 v102, -v104, v102, v104
	v_mul_f32_e32 v101, v102, v101
	v_cvt_pk_bf16_f32 v102, v100, v101
	ds_read_b64 v[100:101], v116 offset:2048
	ds_write_b32 v190, v102 offset:2176
	s_waitcnt lgkmcnt(1)
	v_lshlrev_b32_e32 v104, 16, v100
	v_exp_f32_e32 v104, v104
	v_and_b32_e32 v102, 0xffff0000, v100
	v_lshlrev_b32_e32 v100, 16, v101
	v_fmac_f32_e32 v102, v103, v104
	v_lshlrev_b32_e32 v103, 16, v210
	v_mul_f32_e32 v104, 0x3d372713, v103
	v_mul_f32_e32 v104, v104, v103
	v_fma_f32 v104, v104, v103, v103
	v_mul_f32_e32 v104, 0x40135761, v104
	v_exp_f32_e32 v104, v104
	v_exp_f32_e32 v100, v100
	v_and_b32_e32 v105, 0xffff0000, v101
	v_add_f32_e32 v101, 1.0, v104
	v_and_b32_e32 v104, 0xffff0000, v210
	v_fmac_f32_e32 v105, v106, v100
	v_mul_f32_e32 v106, 0x3d372713, v104
	v_mul_f32_e32 v106, v106, v104
	v_fma_f32 v106, v106, v104, v104
	v_mul_f32_e32 v106, 0x40135761, v106
	v_rcp_f32_e32 v101, v101
	v_exp_f32_e32 v106, v106
	v_fma_f32 v101, -v103, v101, v103
	v_add_f32_e32 v103, 1.0, v106
	v_rcp_f32_e32 v103, v103
	v_lshlrev_b32_e32 v100, 16, v201
	v_add_f32_e32 v100, v102, v100
	v_mul_f32_e32 v100, v101, v100
	v_and_b32_e32 v101, 0xffff0000, v201
	v_add_f32_e32 v101, v105, v101
	v_fma_f32 v103, -v104, v103, v104
	v_mul_f32_e32 v101, v103, v101
	v_cvt_pk_bf16_f32 v103, v100, v101
	ds_read_b64 v[100:101], v116 offset:1920
	ds_write_b32 v190, v103 offset:2048
	s_waitcnt lgkmcnt(1)
	v_lshlrev_b32_e32 v104, 16, v100
	v_exp_f32_e32 v104, v104
	v_and_b32_e32 v103, 0xffff0000, v100
	v_lshlrev_b32_e32 v100, 16, v101
	v_fmac_f32_e32 v103, v102, v104
	v_lshlrev_b32_e32 v102, 16, v208
	v_mul_f32_e32 v104, 0x3d372713, v102
	v_mul_f32_e32 v104, v104, v102
	v_fma_f32 v104, v104, v102, v102
	v_mul_f32_e32 v104, 0x40135761, v104
	v_exp_f32_e32 v104, v104
	v_exp_f32_e32 v100, v100
	v_and_b32_e32 v106, 0xffff0000, v101
	v_add_f32_e32 v101, 1.0, v104
	v_and_b32_e32 v104, 0xffff0000, v208
	v_fmac_f32_e32 v106, v105, v100
	v_mul_f32_e32 v105, 0x3d372713, v104
	v_mul_f32_e32 v105, v105, v104
	v_fma_f32 v105, v105, v104, v104
	v_mul_f32_e32 v105, 0x40135761, v105
	v_rcp_f32_e32 v101, v101
	v_exp_f32_e32 v105, v105
	v_fma_f32 v101, -v102, v101, v102
	v_add_f32_e32 v102, 1.0, v105
	v_rcp_f32_e32 v102, v102
	v_lshlrev_b32_e32 v100, 16, v198
	v_add_f32_e32 v100, v103, v100
	v_mul_f32_e32 v100, v101, v100
	v_and_b32_e32 v101, 0xffff0000, v198
	v_add_f32_e32 v101, v106, v101
	v_fma_f32 v102, -v104, v102, v104
	v_mul_f32_e32 v101, v102, v101
	v_cvt_pk_bf16_f32 v102, v100, v101
	ds_read_b64 v[100:101], v116 offset:1792
	ds_write_b32 v190, v102 offset:1920
	s_waitcnt lgkmcnt(1)
	v_lshlrev_b32_e32 v104, 16, v100
	v_exp_f32_e32 v104, v104
	v_and_b32_e32 v102, 0xffff0000, v100
	v_lshlrev_b32_e32 v100, 16, v101
	v_fmac_f32_e32 v102, v103, v104
	v_lshlrev_b32_e32 v103, 16, v206
	v_mul_f32_e32 v104, 0x3d372713, v103
	v_mul_f32_e32 v104, v104, v103
	v_fma_f32 v104, v104, v103, v103
	v_mul_f32_e32 v104, 0x40135761, v104
	v_exp_f32_e32 v104, v104
	v_exp_f32_e32 v100, v100
	v_and_b32_e32 v105, 0xffff0000, v101
	v_add_f32_e32 v101, 1.0, v104
	v_and_b32_e32 v104, 0xffff0000, v206
	v_fmac_f32_e32 v105, v106, v100
	v_mul_f32_e32 v106, 0x3d372713, v104
	v_mul_f32_e32 v106, v106, v104
	v_fma_f32 v106, v106, v104, v104
	v_mul_f32_e32 v106, 0x40135761, v106
	v_rcp_f32_e32 v101, v101
	v_exp_f32_e32 v106, v106
	v_fma_f32 v101, -v103, v101, v103
	v_add_f32_e32 v103, 1.0, v106
	v_rcp_f32_e32 v103, v103
	v_lshlrev_b32_e32 v100, 16, v196
	v_add_f32_e32 v100, v102, v100
	v_mul_f32_e32 v100, v101, v100
	v_and_b32_e32 v101, 0xffff0000, v196
	v_add_f32_e32 v101, v105, v101
	v_fma_f32 v103, -v104, v103, v104
	v_mul_f32_e32 v101, v103, v101
	v_cvt_pk_bf16_f32 v103, v100, v101
	ds_read_b64 v[100:101], v116 offset:1664
	ds_write_b32 v190, v103 offset:1792
	s_waitcnt lgkmcnt(1)
	v_lshlrev_b32_e32 v104, 16, v100
	v_exp_f32_e32 v104, v104
	v_and_b32_e32 v103, 0xffff0000, v100
	v_lshlrev_b32_e32 v100, 16, v101
	v_fmac_f32_e32 v103, v102, v104
	v_lshlrev_b32_e32 v102, 16, v204
	v_mul_f32_e32 v104, 0x3d372713, v102
	v_mul_f32_e32 v104, v104, v102
	v_fma_f32 v104, v104, v102, v102
	v_mul_f32_e32 v104, 0x40135761, v104
	v_exp_f32_e32 v104, v104
	v_exp_f32_e32 v100, v100
	v_and_b32_e32 v106, 0xffff0000, v101
	v_add_f32_e32 v101, 1.0, v104
	v_and_b32_e32 v104, 0xffff0000, v204
	v_fmac_f32_e32 v106, v105, v100
	v_mul_f32_e32 v105, 0x3d372713, v104
	v_mul_f32_e32 v105, v105, v104
	v_fma_f32 v105, v105, v104, v104
	v_mul_f32_e32 v105, 0x40135761, v105
	v_rcp_f32_e32 v101, v101
	v_exp_f32_e32 v105, v105
	v_fma_f32 v101, -v102, v101, v102
	v_add_f32_e32 v102, 1.0, v105
	v_rcp_f32_e32 v102, v102
	v_lshlrev_b32_e32 v100, 16, v194
	v_add_f32_e32 v100, v103, v100
	v_mul_f32_e32 v100, v101, v100
	v_and_b32_e32 v101, 0xffff0000, v194
	v_add_f32_e32 v101, v106, v101
	v_fma_f32 v102, -v104, v102, v104
	v_mul_f32_e32 v101, v102, v101
	v_cvt_pk_bf16_f32 v102, v100, v101
	ds_read_b64 v[100:101], v116 offset:1536
	ds_write_b32 v190, v102 offset:1664
	s_waitcnt lgkmcnt(1)
	v_lshlrev_b32_e32 v104, 16, v100
	v_exp_f32_e32 v104, v104
	v_and_b32_e32 v102, 0xffff0000, v100
	v_lshlrev_b32_e32 v100, 16, v101
	v_fmac_f32_e32 v102, v103, v104
	v_lshlrev_b32_e32 v103, 16, v202
	v_mul_f32_e32 v104, 0x3d372713, v103
	v_mul_f32_e32 v104, v104, v103
	v_fma_f32 v104, v104, v103, v103
	v_mul_f32_e32 v104, 0x40135761, v104
	v_exp_f32_e32 v104, v104
	v_exp_f32_e32 v100, v100
	v_and_b32_e32 v105, 0xffff0000, v101
	v_add_f32_e32 v101, 1.0, v104
	v_and_b32_e32 v104, 0xffff0000, v202
	v_fmac_f32_e32 v105, v106, v100
	v_mul_f32_e32 v106, 0x3d372713, v104
	v_mul_f32_e32 v106, v106, v104
	v_fma_f32 v106, v106, v104, v104
	v_mul_f32_e32 v106, 0x40135761, v106
	v_rcp_f32_e32 v101, v101
	v_exp_f32_e32 v106, v106
	v_fma_f32 v101, -v103, v101, v103
	v_add_f32_e32 v103, 1.0, v106
	v_rcp_f32_e32 v103, v103
	v_lshlrev_b32_e32 v100, 16, v157
	v_add_f32_e32 v100, v102, v100
	v_mul_f32_e32 v100, v101, v100
	v_and_b32_e32 v101, 0xffff0000, v157
	v_add_f32_e32 v101, v105, v101
	v_fma_f32 v103, -v104, v103, v104
	v_mul_f32_e32 v101, v103, v101
	v_cvt_pk_bf16_f32 v103, v100, v101
	ds_read_b64 v[100:101], v116 offset:1408
	ds_write_b32 v190, v103 offset:1536
	s_waitcnt lgkmcnt(1)
	v_lshlrev_b32_e32 v104, 16, v100
	v_exp_f32_e32 v104, v104
	v_and_b32_e32 v103, 0xffff0000, v100
	v_lshlrev_b32_e32 v100, 16, v101
	v_fmac_f32_e32 v103, v102, v104
	v_lshlrev_b32_e32 v102, 16, v200
	v_mul_f32_e32 v104, 0x3d372713, v102
	v_mul_f32_e32 v104, v104, v102
	v_fma_f32 v104, v104, v102, v102
	v_mul_f32_e32 v104, 0x40135761, v104
	v_exp_f32_e32 v104, v104
	v_exp_f32_e32 v100, v100
	v_and_b32_e32 v106, 0xffff0000, v101
	v_add_f32_e32 v101, 1.0, v104
	v_and_b32_e32 v104, 0xffff0000, v200
	v_fmac_f32_e32 v106, v105, v100
	v_mul_f32_e32 v105, 0x3d372713, v104
	v_mul_f32_e32 v105, v105, v104
	v_fma_f32 v105, v105, v104, v104
	v_mul_f32_e32 v105, 0x40135761, v105
	v_rcp_f32_e32 v101, v101
	v_exp_f32_e32 v105, v105
	v_fma_f32 v101, -v102, v101, v102
	v_add_f32_e32 v102, 1.0, v105
	v_rcp_f32_e32 v102, v102
	v_lshlrev_b32_e32 v100, 16, v155
	v_add_f32_e32 v100, v103, v100
	v_mul_f32_e32 v100, v101, v100
	v_and_b32_e32 v101, 0xffff0000, v155
	v_add_f32_e32 v101, v106, v101
	v_fma_f32 v102, -v104, v102, v104
	v_mul_f32_e32 v101, v102, v101
	v_cvt_pk_bf16_f32 v102, v100, v101
	ds_read_b64 v[100:101], v116 offset:1280
	ds_write_b32 v190, v102 offset:1408
	s_waitcnt lgkmcnt(1)
	v_lshlrev_b32_e32 v104, 16, v100
	v_exp_f32_e32 v104, v104
	v_and_b32_e32 v102, 0xffff0000, v100
	v_lshlrev_b32_e32 v100, 16, v101
	v_fmac_f32_e32 v102, v103, v104
	v_lshlrev_b32_e32 v103, 16, v199
	v_mul_f32_e32 v104, 0x3d372713, v103
	v_mul_f32_e32 v104, v104, v103
	v_fma_f32 v104, v104, v103, v103
	v_mul_f32_e32 v104, 0x40135761, v104
	v_exp_f32_e32 v104, v104
	v_exp_f32_e32 v100, v100
	v_and_b32_e32 v105, 0xffff0000, v101
	v_add_f32_e32 v101, 1.0, v104
	v_and_b32_e32 v104, 0xffff0000, v199
	v_fmac_f32_e32 v105, v106, v100
	v_mul_f32_e32 v106, 0x3d372713, v104
	v_mul_f32_e32 v106, v106, v104
	v_fma_f32 v106, v106, v104, v104
	v_mul_f32_e32 v106, 0x40135761, v106
	v_rcp_f32_e32 v101, v101
	v_exp_f32_e32 v106, v106
	v_fma_f32 v101, -v103, v101, v103
	v_add_f32_e32 v103, 1.0, v106
	v_rcp_f32_e32 v103, v103
	v_lshlrev_b32_e32 v100, 16, v152
	v_add_f32_e32 v100, v102, v100
	v_mul_f32_e32 v100, v101, v100
	v_and_b32_e32 v101, 0xffff0000, v152
	v_add_f32_e32 v101, v105, v101
	v_fma_f32 v103, -v104, v103, v104
	v_mul_f32_e32 v101, v103, v101
	v_cvt_pk_bf16_f32 v103, v100, v101
	ds_read_b64 v[100:101], v116 offset:1152
	ds_write_b32 v190, v103 offset:1280
	s_waitcnt lgkmcnt(1)
	v_lshlrev_b32_e32 v104, 16, v100
	v_exp_f32_e32 v104, v104
	v_and_b32_e32 v103, 0xffff0000, v100
	v_lshlrev_b32_e32 v100, 16, v101
	v_fmac_f32_e32 v103, v102, v104
	v_lshlrev_b32_e32 v102, 16, v197
	v_mul_f32_e32 v104, 0x3d372713, v102
	v_mul_f32_e32 v104, v104, v102
	v_fma_f32 v104, v104, v102, v102
	v_mul_f32_e32 v104, 0x40135761, v104
	v_exp_f32_e32 v104, v104
	v_exp_f32_e32 v100, v100
	v_and_b32_e32 v106, 0xffff0000, v101
	v_add_f32_e32 v101, 1.0, v104
	v_and_b32_e32 v104, 0xffff0000, v197
	v_fmac_f32_e32 v106, v105, v100
	v_mul_f32_e32 v105, 0x3d372713, v104
	v_mul_f32_e32 v105, v105, v104
	v_fma_f32 v105, v105, v104, v104
	v_mul_f32_e32 v105, 0x40135761, v105
	v_rcp_f32_e32 v101, v101
	v_exp_f32_e32 v105, v105
	v_fma_f32 v101, -v102, v101, v102
	v_add_f32_e32 v102, 1.0, v105
	v_rcp_f32_e32 v102, v102
	v_lshlrev_b32_e32 v100, 16, v150
	v_add_f32_e32 v100, v103, v100
	v_mul_f32_e32 v100, v101, v100
	v_and_b32_e32 v101, 0xffff0000, v150
	v_add_f32_e32 v101, v106, v101
	v_fma_f32 v102, -v104, v102, v104
	v_mul_f32_e32 v101, v102, v101
	v_cvt_pk_bf16_f32 v102, v100, v101
	ds_read_b64 v[100:101], v116 offset:1024
	ds_write_b32 v190, v102 offset:1152
	s_waitcnt lgkmcnt(1)
	v_lshlrev_b32_e32 v104, 16, v100
	v_exp_f32_e32 v104, v104
	v_and_b32_e32 v102, 0xffff0000, v100
	v_lshlrev_b32_e32 v100, 16, v101
	v_fmac_f32_e32 v102, v103, v104
	v_lshlrev_b32_e32 v103, 16, v195
	v_mul_f32_e32 v104, 0x3d372713, v103
	v_mul_f32_e32 v104, v104, v103
	v_fma_f32 v104, v104, v103, v103
	v_mul_f32_e32 v104, 0x40135761, v104
	v_exp_f32_e32 v104, v104
	v_exp_f32_e32 v100, v100
	v_and_b32_e32 v105, 0xffff0000, v101
	v_add_f32_e32 v101, 1.0, v104
	v_and_b32_e32 v104, 0xffff0000, v195
	v_fmac_f32_e32 v105, v106, v100
	v_mul_f32_e32 v106, 0x3d372713, v104
	v_mul_f32_e32 v106, v106, v104
	v_fma_f32 v106, v106, v104, v104
	v_mul_f32_e32 v106, 0x40135761, v106
	v_rcp_f32_e32 v101, v101
	v_exp_f32_e32 v106, v106
	v_fma_f32 v101, -v103, v101, v103
	v_add_f32_e32 v103, 1.0, v106
	v_rcp_f32_e32 v103, v103
	v_lshlrev_b32_e32 v100, 16, v148
	v_add_f32_e32 v100, v102, v100
	v_mul_f32_e32 v100, v101, v100
	v_and_b32_e32 v101, 0xffff0000, v148
	v_add_f32_e32 v101, v105, v101
	v_fma_f32 v103, -v104, v103, v104
	v_mul_f32_e32 v101, v103, v101
	v_cvt_pk_bf16_f32 v103, v100, v101
	ds_read_b64 v[100:101], v116 offset:896
	ds_write_b32 v190, v103 offset:1024
	s_waitcnt lgkmcnt(1)
	v_lshlrev_b32_e32 v104, 16, v100
	v_exp_f32_e32 v104, v104
	v_and_b32_e32 v103, 0xffff0000, v100
	v_lshlrev_b32_e32 v100, 16, v101
	v_fmac_f32_e32 v103, v102, v104
	v_lshlrev_b32_e32 v102, 16, v193
	v_mul_f32_e32 v104, 0x3d372713, v102
	v_mul_f32_e32 v104, v104, v102
	v_fma_f32 v104, v104, v102, v102
	v_mul_f32_e32 v104, 0x40135761, v104
	v_exp_f32_e32 v104, v104
	v_exp_f32_e32 v100, v100
	v_and_b32_e32 v106, 0xffff0000, v101
	v_add_f32_e32 v101, 1.0, v104
	v_and_b32_e32 v104, 0xffff0000, v193
	v_fmac_f32_e32 v106, v105, v100
	v_mul_f32_e32 v105, 0x3d372713, v104
	v_mul_f32_e32 v105, v105, v104
	v_fma_f32 v105, v105, v104, v104
	v_mul_f32_e32 v105, 0x40135761, v105
	v_rcp_f32_e32 v101, v101
	v_exp_f32_e32 v105, v105
	v_fma_f32 v101, -v102, v101, v102
	v_add_f32_e32 v102, 1.0, v105
	v_rcp_f32_e32 v102, v102
	v_lshlrev_b32_e32 v100, 16, v146
	v_add_f32_e32 v100, v103, v100
	v_mul_f32_e32 v100, v101, v100
	v_and_b32_e32 v101, 0xffff0000, v146
	v_add_f32_e32 v101, v106, v101
	v_fma_f32 v102, -v104, v102, v104
	v_mul_f32_e32 v101, v102, v101
	v_cvt_pk_bf16_f32 v102, v100, v101
	ds_read_b64 v[100:101], v116 offset:768
	ds_write_b32 v190, v102 offset:896
	s_waitcnt lgkmcnt(1)
	v_lshlrev_b32_e32 v104, 16, v100
	v_exp_f32_e32 v104, v104
	v_and_b32_e32 v102, 0xffff0000, v100
	v_lshlrev_b32_e32 v100, 16, v101
	v_fmac_f32_e32 v102, v103, v104
	v_lshlrev_b32_e32 v103, 16, v156
	v_mul_f32_e32 v104, 0x3d372713, v103
	v_mul_f32_e32 v104, v104, v103
	v_fma_f32 v104, v104, v103, v103
	v_mul_f32_e32 v104, 0x40135761, v104
	v_exp_f32_e32 v104, v104
	v_exp_f32_e32 v100, v100
	v_and_b32_e32 v105, 0xffff0000, v101
	v_add_f32_e32 v101, 1.0, v104
	v_and_b32_e32 v104, 0xffff0000, v156
	v_fmac_f32_e32 v105, v106, v100
	v_mul_f32_e32 v106, 0x3d372713, v104
	v_mul_f32_e32 v106, v106, v104
	v_fma_f32 v106, v106, v104, v104
	v_mul_f32_e32 v106, 0x40135761, v106
	v_rcp_f32_e32 v101, v101
	v_exp_f32_e32 v106, v106
	v_fma_f32 v101, -v103, v101, v103
	v_add_f32_e32 v103, 1.0, v106
	v_rcp_f32_e32 v103, v103
	v_lshlrev_b32_e32 v100, 16, v144
	v_add_f32_e32 v100, v102, v100
	v_mul_f32_e32 v100, v101, v100
	v_and_b32_e32 v101, 0xffff0000, v144
	v_add_f32_e32 v101, v105, v101
	v_fma_f32 v103, -v104, v103, v104
	v_mul_f32_e32 v101, v103, v101
	v_cvt_pk_bf16_f32 v103, v100, v101
	ds_read_b64 v[100:101], v116 offset:640
	ds_write_b32 v190, v103 offset:768
	s_waitcnt lgkmcnt(1)
	v_lshlrev_b32_e32 v104, 16, v100
	v_exp_f32_e32 v104, v104
	v_and_b32_e32 v103, 0xffff0000, v100
	v_lshlrev_b32_e32 v100, 16, v101
	v_fmac_f32_e32 v103, v102, v104
	v_lshlrev_b32_e32 v102, 16, v154
	v_mul_f32_e32 v104, 0x3d372713, v102
	v_mul_f32_e32 v104, v104, v102
	v_fma_f32 v104, v104, v102, v102
	v_mul_f32_e32 v104, 0x40135761, v104
	v_exp_f32_e32 v104, v104
	v_exp_f32_e32 v100, v100
	v_and_b32_e32 v106, 0xffff0000, v101
	v_add_f32_e32 v101, 1.0, v104
	v_and_b32_e32 v104, 0xffff0000, v154
	v_fmac_f32_e32 v106, v105, v100
	v_mul_f32_e32 v105, 0x3d372713, v104
	v_mul_f32_e32 v105, v105, v104
	v_fma_f32 v105, v105, v104, v104
	v_mul_f32_e32 v105, 0x40135761, v105
	v_rcp_f32_e32 v101, v101
	v_exp_f32_e32 v105, v105
	v_fma_f32 v101, -v102, v101, v102
	v_add_f32_e32 v102, 1.0, v105
	v_rcp_f32_e32 v102, v102
	v_lshlrev_b32_e32 v100, 16, v143
	v_add_f32_e32 v100, v103, v100
	v_mul_f32_e32 v100, v101, v100
	v_and_b32_e32 v101, 0xffff0000, v143
	v_add_f32_e32 v101, v106, v101
	v_fma_f32 v102, -v104, v102, v104
	v_mul_f32_e32 v101, v102, v101
	v_cvt_pk_bf16_f32 v102, v100, v101
	ds_read_b64 v[100:101], v116 offset:512
	ds_write_b32 v190, v102 offset:640
	s_waitcnt lgkmcnt(1)
	v_lshlrev_b32_e32 v104, 16, v100
	v_exp_f32_e32 v104, v104
	v_and_b32_e32 v102, 0xffff0000, v100
	v_lshlrev_b32_e32 v100, 16, v101
	v_fmac_f32_e32 v102, v103, v104
	v_lshlrev_b32_e32 v103, 16, v153
	v_mul_f32_e32 v104, 0x3d372713, v103
	v_mul_f32_e32 v104, v104, v103
	v_fma_f32 v104, v104, v103, v103
	v_mul_f32_e32 v104, 0x40135761, v104
	v_exp_f32_e32 v104, v104
	v_exp_f32_e32 v100, v100
	v_and_b32_e32 v105, 0xffff0000, v101
	v_add_f32_e32 v101, 1.0, v104
	v_and_b32_e32 v104, 0xffff0000, v153
	v_fmac_f32_e32 v105, v106, v100
	v_mul_f32_e32 v106, 0x3d372713, v104
	v_mul_f32_e32 v106, v106, v104
	v_fma_f32 v106, v106, v104, v104
	v_mul_f32_e32 v106, 0x40135761, v106
	v_rcp_f32_e32 v101, v101
	v_exp_f32_e32 v106, v106
	v_fma_f32 v101, -v103, v101, v103
	v_add_f32_e32 v103, 1.0, v106
	v_rcp_f32_e32 v103, v103
	v_lshlrev_b32_e32 v100, 16, v142
	v_add_f32_e32 v100, v102, v100
	v_mul_f32_e32 v100, v101, v100
	v_and_b32_e32 v101, 0xffff0000, v142
	v_add_f32_e32 v101, v105, v101
	v_fma_f32 v103, -v104, v103, v104
	v_mul_f32_e32 v101, v103, v101
	v_cvt_pk_bf16_f32 v103, v100, v101
	ds_read_b64 v[100:101], v116 offset:384
	ds_write_b32 v190, v103 offset:512
	s_waitcnt lgkmcnt(1)
	v_lshlrev_b32_e32 v104, 16, v100
	v_exp_f32_e32 v104, v104
	v_and_b32_e32 v103, 0xffff0000, v100
	v_lshlrev_b32_e32 v100, 16, v101
	v_fmac_f32_e32 v103, v102, v104
	v_lshlrev_b32_e32 v102, 16, v151
	v_mul_f32_e32 v104, 0x3d372713, v102
	v_mul_f32_e32 v104, v104, v102
	v_fma_f32 v104, v104, v102, v102
	v_mul_f32_e32 v104, 0x40135761, v104
	v_exp_f32_e32 v104, v104
	v_exp_f32_e32 v100, v100
	v_and_b32_e32 v106, 0xffff0000, v101
	v_add_f32_e32 v101, 1.0, v104
	v_and_b32_e32 v104, 0xffff0000, v151
	v_fmac_f32_e32 v106, v105, v100
	v_mul_f32_e32 v105, 0x3d372713, v104
	v_mul_f32_e32 v105, v105, v104
	v_fma_f32 v105, v105, v104, v104
	v_mul_f32_e32 v105, 0x40135761, v105
	v_rcp_f32_e32 v101, v101
	v_exp_f32_e32 v105, v105
	v_fma_f32 v101, -v102, v101, v102
	v_add_f32_e32 v102, 1.0, v105
	v_rcp_f32_e32 v102, v102
	v_lshlrev_b32_e32 v100, 16, v141
	v_add_f32_e32 v100, v103, v100
	v_mul_f32_e32 v100, v101, v100
	v_and_b32_e32 v101, 0xffff0000, v141
	v_add_f32_e32 v101, v106, v101
	v_fma_f32 v102, -v104, v102, v104
	v_mul_f32_e32 v101, v102, v101
	v_cvt_pk_bf16_f32 v102, v100, v101
	ds_read_b64 v[100:101], v116 offset:256
	ds_write_b32 v190, v102 offset:384
	s_waitcnt lgkmcnt(1)
	v_lshlrev_b32_e32 v104, 16, v100
	v_exp_f32_e32 v104, v104
	v_and_b32_e32 v102, 0xffff0000, v100
	v_lshlrev_b32_e32 v100, 16, v101
	v_fmac_f32_e32 v102, v103, v104
	v_lshlrev_b32_e32 v103, 16, v149
	v_mul_f32_e32 v104, 0x3d372713, v103
	v_mul_f32_e32 v104, v104, v103
	v_fma_f32 v104, v104, v103, v103
	v_mul_f32_e32 v104, 0x40135761, v104
	v_exp_f32_e32 v104, v104
	v_exp_f32_e32 v100, v100
	v_and_b32_e32 v105, 0xffff0000, v101
	v_add_f32_e32 v101, 1.0, v104
	v_and_b32_e32 v104, 0xffff0000, v149
	v_fmac_f32_e32 v105, v106, v100
	v_mul_f32_e32 v106, 0x3d372713, v104
	v_mul_f32_e32 v106, v106, v104
	v_fma_f32 v106, v106, v104, v104
	v_mul_f32_e32 v106, 0x40135761, v106
	v_rcp_f32_e32 v101, v101
	v_exp_f32_e32 v106, v106
	v_fma_f32 v101, -v103, v101, v103
	v_add_f32_e32 v103, 1.0, v106
	v_rcp_f32_e32 v103, v103
	v_lshlrev_b32_e32 v100, 16, v140
	v_add_f32_e32 v100, v102, v100
	v_mul_f32_e32 v100, v101, v100
	v_and_b32_e32 v101, 0xffff0000, v140
	v_add_f32_e32 v101, v105, v101
	v_fma_f32 v103, -v104, v103, v104
	v_mul_f32_e32 v101, v103, v101
	v_cvt_pk_bf16_f32 v103, v100, v101
	ds_read_b64 v[100:101], v116 offset:128
	ds_write_b32 v190, v103 offset:256
	s_waitcnt lgkmcnt(1)
	v_lshlrev_b32_e32 v104, 16, v100
	v_exp_f32_e32 v104, v104
	v_and_b32_e32 v103, 0xffff0000, v100
	v_lshlrev_b32_e32 v100, 16, v101
	v_fmac_f32_e32 v103, v102, v104
	v_lshlrev_b32_e32 v102, 16, v147
	v_mul_f32_e32 v104, 0x3d372713, v102
	v_mul_f32_e32 v104, v104, v102
	v_fma_f32 v104, v104, v102, v102
	v_mul_f32_e32 v104, 0x40135761, v104
	v_exp_f32_e32 v104, v104
	v_exp_f32_e32 v100, v100
	v_and_b32_e32 v106, 0xffff0000, v101
	v_add_f32_e32 v101, 1.0, v104
	v_and_b32_e32 v104, 0xffff0000, v147
	v_fmac_f32_e32 v106, v105, v100
	v_mul_f32_e32 v105, 0x3d372713, v104
	v_mul_f32_e32 v105, v105, v104
	v_fma_f32 v105, v105, v104, v104
	v_mul_f32_e32 v105, 0x40135761, v105
	v_rcp_f32_e32 v101, v101
	v_exp_f32_e32 v105, v105
	v_fma_f32 v101, -v102, v101, v102
	v_add_f32_e32 v102, 1.0, v105
	v_rcp_f32_e32 v102, v102
	v_lshlrev_b32_e32 v100, 16, v139
	v_add_f32_e32 v100, v103, v100
	v_mul_f32_e32 v100, v101, v100
	v_and_b32_e32 v101, 0xffff0000, v139
	v_add_f32_e32 v101, v106, v101
	v_fma_f32 v102, -v104, v102, v104
	v_mul_f32_e32 v101, v102, v101
	v_cvt_pk_bf16_f32 v102, v100, v101
	ds_read_b64 v[100:101], v116
	ds_write_b32 v190, v102 offset:128
	s_waitcnt lgkmcnt(1)
	v_lshlrev_b32_e32 v104, 16, v100
	v_exp_f32_e32 v104, v104
	v_and_b32_e32 v100, 0xffff0000, v100
	v_lshlrev_b32_e32 v102, 16, v101
	v_fmac_f32_e32 v100, v103, v104
	v_lshlrev_b32_e32 v103, 16, v145
	v_mul_f32_e32 v104, 0x3d372713, v103
	v_mul_f32_e32 v104, v104, v103
	v_fma_f32 v104, v104, v103, v103
	v_mul_f32_e32 v104, 0x3f4c422a, v104
	v_add_f32_e32 v104, v104, v104
	v_mul_f32_e32 v104, 0x3fb8aa3b, v104
	v_exp_f32_e32 v104, v104
	v_exp_f32_e32 v102, v102
	v_and_b32_e32 v101, 0xffff0000, v101
	v_mul_f32_e32 v103, 0.5, v103
	v_add_f32_e32 v104, 1.0, v104
	v_rcp_f32_e32 v104, v104
	v_fmac_f32_e32 v101, v106, v102
	v_lshlrev_b32_e32 v102, 16, v138
	v_add_f32_e32 v100, v100, v102
	v_fma_f32 v102, v104, -2.0, 1.0
	v_and_b32_e32 v104, 0xffff0000, v145
	v_mul_f32_e32 v105, 0x3d372713, v104
	v_mul_f32_e32 v105, v105, v104
	v_fma_f32 v105, v105, v104, v104
	v_mul_f32_e32 v105, 0x3f4c422a, v105
	v_add_f32_e32 v105, v105, v105
	v_mul_f32_e32 v105, 0x3fb8aa3b, v105
	v_exp_f32_e32 v105, v105
	v_add_f32_e32 v102, 1.0, v102
	v_mul_f32_e32 v102, v103, v102
	v_mul_f32_e32 v100, v102, v100
	v_add_f32_e32 v103, 1.0, v105
	v_rcp_f32_e32 v103, v103
	v_and_b32_e32 v102, 0xffff0000, v138
	v_add_f32_e32 v101, v101, v102
	v_fma_f32 v102, v103, -2.0, 1.0
	v_mul_f32_e32 v103, 0.5, v104
	v_add_f32_e32 v102, 1.0, v102
	v_mul_f32_e32 v102, v103, v102
	v_mul_f32_e32 v101, v102, v101
	v_cvt_pk_bf16_f32 v100, v100, v101
	ds_write_b32 v190, v100
	v_or_b32_e32 v102, s44, v72
	v_mov_b64_e32 v[100:101], s[20:21]
	v_mad_u64_u32 v[100:101], s[48:49], v102, s52, v[100:101]
	v_mad_i32_i24 v101, s45, v192, v101
	v_lshl_add_u64 v[100:101], s[42:43], 1, v[100:101]
	v_lshl_add_u64 v[100:101], v[100:101], 0, s[36:37]
	v_lshl_add_u64 v[104:105], v[100:101], 0, v[70:71]
	ds_read_b128 v[100:103], v191
	s_waitcnt lgkmcnt(0)
	global_store_dwordx4 v[104:105], v[100:103], off
	v_lshl_add_u64 v[104:105], v[104:105], 0, s[40:41]
	ds_read_b128 v[100:103], v191 offset:2048
	s_waitcnt lgkmcnt(0)
	global_store_dwordx4 v[104:105], v[100:103], off
	v_lshl_add_u64 v[104:105], v[104:105], 0, s[40:41]
	ds_read_b128 v[100:103], v191 offset:4224
	s_waitcnt lgkmcnt(0)
	global_store_dwordx4 v[104:105], v[100:103], off
	v_lshl_add_u64 v[104:105], v[104:105], 0, s[40:41]
	ds_read_b128 v[100:103], v191 offset:6272
	s_waitcnt lgkmcnt(0)
	global_store_dwordx4 v[104:105], v[100:103], off
	v_lshl_add_u64 v[104:105], v[104:105], 0, s[40:41]
	ds_read_b128 v[100:103], v191 offset:8448
	s_waitcnt lgkmcnt(0)
	global_store_dwordx4 v[104:105], v[100:103], off
	v_lshl_add_u64 v[104:105], v[104:105], 0, s[40:41]
	ds_read_b128 v[100:103], v191 offset:10496
	s_waitcnt lgkmcnt(0)
	global_store_dwordx4 v[104:105], v[100:103], off
	v_lshl_add_u64 v[104:105], v[104:105], 0, s[40:41]
	ds_read_b128 v[100:103], v191 offset:12672
	s_waitcnt lgkmcnt(0)
	global_store_dwordx4 v[104:105], v[100:103], off
	v_lshl_add_u64 v[104:105], v[104:105], 0, s[40:41]
	ds_read_b128 v[100:103], v191 offset:14720
	s_waitcnt lgkmcnt(0)
	global_store_dwordx4 v[104:105], v[100:103], off
	s_cbranch_vccz .LBB0_1505
